# MoE gate/up tiles: store drain + barrier + slot-tile flag deferred into the next tile's first drain/barrier (or before the first down tile / end of list)
# speedup vs baseline: 1.0073x; 1.0002x over previous
; #define LAS __attribute__((address_space(3)))
; __device__ __forceinline__ void ph_moe2_mfma(const Ctx& c, int layer, int tile, const int* sm, unsigned char* lds) {
;     const int st = tile >> 3, nt = tile & 7;
;     const int s0 = st * 128;
;     if (s0 >= sm[32]) return;
;     const int e = slot_expert(sm, s0), base = s0 - sm[e], ce = sm[33 + e];
;     if (base >= ce) return;
; __global__ void __launch_bounds__(NTHR, 2) mk_fwd(Params prm) {
;     ...
;             case 7: { moe_offsets(c, layer, smi);
;                       const int n1v = (__builtin_amdgcn_readfirstlane(((const LAS int*)smi)[32]) >> 7) * 8;
;                       for (int t = bid; t < 2 * n1v; t += G) { asm volatile("" : "+v"(c.tid)); asm volatile("" : "+s"(c.p)); if (t < n1v) ph_moe1_mfma(c, layer, t, smi, smem_raw); else ph_moe2_mfma(c, layer, t - n1v, smi, smem_raw); } } break;
.LBB0_137:
	v_writelane_b32 v254, s59, 1
	s_lshr_b32 s16, s55, 3
	s_cmp_ge_i32 s59, s55
	s_cselect_b32 s6, s55, 0
	s_sub_i32 s7, s59, s6
	s_and_b32 s15, s7, 7
	s_lshr_b32 s7, s7, 3
	s_mul_i32 s15, s15, s16
	s_add_i32 s7, s7, s15
	s_add_i32 s59, s7, s6
	s_mov_b32 s58, s59
	ds_read_b32 v2, v3 offset:36032
	s_cmp_ge_i32 s59, s55
	s_mov_b64 s[6:7], -1
	s_waitcnt lgkmcnt(0)
	v_readfirstlane_b32 s15, v2
	s_cbranch_scc0 .LBB0_154
	s_cmp_eq_u32 s101, 0
	s_cbranch_scc1 .Lm1_nopend2
	s_waitcnt vmcnt(0)
	s_barrier
	s_lshl_b32 s50, s100, 2
	s_add_u32 s50, s42, s50
	s_addc_u32 s51, s43, 0
	v_cmp_eq_u32_e32 vcc, 0, v118
	s_and_saveexec_b64 s[48:49], vcc
	v_mov_b32_e32 v2, 1
	global_atomic_add v221, v2, s[50:51]
	s_mov_b64 exec, s[48:49]
	s_mov_b32 s101, 0
.Lm1_nopend2:
	s_sub_i32 s6, s59, s55
	s_lshr_b32 s16, s6, 3
	s_lshl_b32 s72, s16, 7
	s_cmp_ge_i32 s72, s15
	s_cbranch_scc1 .LBB0_153
	s_mov_b64 s[6:7], 0
	s_mov_b64 s[28:29], exec
	v_readlane_b32 s18, v253, 17
	v_readlane_b32 s19, v253, 18
	s_and_b64 s[18:19], s[28:29], s[18:19]
	s_mov_b64 exec, s[18:19]
	s_cbranch_execz .LBB0_141
	ds_read_b32 v2, v1 offset:35904
	s_waitcnt lgkmcnt(0)
	v_cmp_ge_i32_e32 vcc, s72, v2
	s_and_b64 s[6:7], vcc, exec

;     template <class T> __device__ __forceinline__ T* w(size_t off) const { return (T*)(p->ws + off); }
;     ...
;     unsigned ao[4];
; #pragma unroll
;     for (int i = 0; i < 4; ++i) ao[i] = arow((tid >> 3) + 32 * i) + (tid & 7) * 8;
;     const int bk = tid >> 4, bnc = tid & 15;
;     constexpr int NRB = B_F32 ? 8 : 4;
;     u32x4 ra0[4], ra1[4]; u32x4 rb0[NRB], rb1[NRB];
;     auto gloadA = [&](int kt, u32x4 (&ra)[4]) __attribute__((always_inline)) {
; #pragma unroll
;         for (int i = 0; i < 4; ++i) ra[i] = *(const u32x4*)(Abase + (ao[i] + kt * 64));
;     };
;     auto gloadB = [&](int kt, u32x4 (&rb)[NRB]) __attribute__((always_inline)) {
;         if (B_F32) {
;             const float* bp = (const float*)Bbase + (boff + (unsigned)((kt * 64 + bk) * ldb));
; #pragma unroll
;             for (int i = 0; i < 4; ++i) {
;                 if (bval) { rb[2 * i] = *(const u32x4*)(bp + (unsigned)(16 * i * ldb)); rb[2 * i + 1] = *(const u32x4*)(bp + (unsigned)(16 * i * ldb) + 4); }
;                 else { rb[2 * i] = (u32x4){0u, 0u, 0u, 0u}; rb[2 * i + 1] = rb[2 * i]; }
;             }
;         } else {
;             const bf16* bp = (const bf16*)Bbase + (boff + (unsigned)((kt * 64 + bk) * ldb));
; #pragma unroll
;             for (int i = 0; i < 4; ++i) rb[i] = bval ? *(const u32x4*)(bp + (unsigned)(16 * i * ldb)) : (u32x4){0u, 0u, 0u, 0u};
;         }
;     };
;     auto lstore = [&](const u32x4 (&ra)[4], const u32x4 (&rb)[NRB]) __attribute__((always_inline)) {
; #pragma unroll
;         for (int i = 0; i < 4; ++i) { const int row = (tid >> 3) + 32 * i, kc = tid & 7;
;             const u32x4 v = (kc & 1) ? (u32x4){ra[i][2], ra[i][3], ra[i][0], ra[i][1]} : ra[i];
;             *(u32x4*)(lds + (kc >> 2) * GA_KH + row * 64 + (kc & 3) * 16) = v; }
; #pragma unroll
;         for (int i = 0; i < 4; ++i) { const int k = bk + 16 * i;
;             u32x4 v;
; __device__ __forceinline__ void ph_moe1_mfma(const Ctx& c, int layer, int tile, const int* sm, unsigned char* lds) {
;     ...
;     const bf16* HA = c.w<bf16>(WS_HA); const int* LI = c.w<int>(WS_LIST) + (size_t)e * NT;
;     f32x4 acc[4][4];
;     gemm_tile<false>(c.tid, lds, HA, [&](int r) __attribute__((always_inline)) { const int tok = LI[(base + r < ce) ? (base + r) : base]; return (unsigned)(tok * D); }, c.w<bf16>(WS_BGU) + (size_t)e * D * 1024, (unsigned)(nt * 128 + (c.tid & 15) * 8), 1024, true, D, acc);
.LBB0_162:
	s_and_b32 s7, s58, 7
	s_and_b32 s6, s59, 7
	s_lshl_b32 s15, s7, 7
	v_ashrrev_i32_e32 v4, 3, v118
	s_add_u32 s28, s42, 0x45c6000
	v_add_u32_e32 v4, v2, v4
	s_addc_u32 s29, s43, 0
	s_mul_i32 s7, s18, 0x11000
	v_cmp_lt_i32_e32 vcc, v4, v5
	v_add_u32_e32 v8, 32, v4
	s_add_u32 s7, s42, s7
	v_cndmask_b32_e32 v6, v2, v4, vcc
	v_cmp_lt_i32_e32 vcc, v8, v5
	v_add_u32_e32 v10, 64, v4
	s_addc_u32 s19, s43, 0
	v_cndmask_b32_e32 v8, v2, v8, vcc
	v_cmp_lt_i32_e32 vcc, v10, v5
	v_add_u32_e32 v4, 0x60, v4
	s_add_u32 s44, s7, 0x1012c000
	v_cndmask_b32_e32 v10, v2, v10, vcc
	v_cmp_lt_i32_e32 vcc, v4, v5
	s_addc_u32 s45, s19, 0
	v_ashrrev_i32_e32 v7, 31, v6
	v_cndmask_b32_e32 v4, v2, v4, vcc
	v_lshl_add_u64 v[6:7], v[6:7], 2, s[44:45]
	v_ashrrev_i32_e32 v9, 31, v8
	v_ashrrev_i32_e32 v11, 31, v10
	v_ashrrev_i32_e32 v5, 31, v4
	v_lshl_add_u64 v[8:9], v[8:9], 2, s[44:45]
	v_lshl_add_u64 v[10:11], v[10:11], 2, s[44:45]
	v_lshl_add_u64 v[4:5], v[4:5], 2, s[44:45]
	global_load_dword v12, v[6:7], off
	global_load_dword v13, v[8:9], off
	global_load_dword v14, v[10:11], off
	global_load_dword v15, v[4:5], off
	s_lshl_b32 s18, s18, 21
	v_bfe_u32 v2, v118, 4, 2
	v_ashrrev_i32_e32 v4, 1, v118
	v_bfe_u32 v6, v118, 4, 1
	s_add_u32 s18, s42, s18
	v_bfe_u32 v5, v118, 2, 2
	v_lshlrev_b32_e32 v7, 1, v118
	v_and_b32_e32 v120, 0xffffffc0, v4
	v_lshlrev_b32_e32 v19, 4, v2
	v_lshlrev_b32_e32 v2, 3, v2
	v_lshlrev_b32_e32 v4, 2, v6
	s_addc_u32 s19, s43, 0
	v_lshlrev_b32_e32 v16, 3, v118
	v_ashrrev_i32_e32 v17, 4, v118
	v_and_b32_e32 v7, 0x80, v7
	v_or3_b32 v2, v2, v5, v4
	s_movk_i32 s48, 0x120
	s_add_u32 s44, s18, 0x18dd5100
	v_and_b32_e32 v18, 0x78, v16
	v_lshlrev_b32_e32 v21, 10, v17
	v_mad_u32_u24 v2, v2, s48, v7
	s_addc_u32 s45, s19, 0
	s_lshl_b32 s18, s6, 7
	v_and_b32_e32 v119, 15, v118
	v_and_or_b32 v122, v16, 24, v2
	v_or3_b32 v2, v18, s18, v21
	v_cmp_eq_u32_e32 vcc, 0, v6
	v_or_b32_e32 v6, v120, v119
	v_lshl_add_u64 v[4:5], v[2:3], 1, s[44:45]
	v_cndmask_b32_e32 v20, v236, v237, vcc
	v_lshlrev_b32_e32 v22, 6, v6
	v_add_co_u32_e32 v6, vcc, s40, v4
	s_mov_b32 s18, 0x10000
	s_nop 0
	v_addc_co_u32_e32 v7, vcc, 0, v5, vcc
	v_add_co_u32_e32 v8, vcc, s18, v4
	s_mov_b32 s19, 0x18000
	s_nop 0
	v_addc_co_u32_e32 v9, vcc, 0, v5, vcc
	v_and_b32_e32 v121, 56, v16
	v_add_co_u32_e32 v10, vcc, s19, v4
	v_add_u32_e32 v2, 0x10000, v2
	s_nop 0
	v_addc_co_u32_e32 v11, vcc, 0, v5, vcc
	v_mov_b32_e32 v5, v3
	v_mov_b32_e32 v7, v3
	v_mov_b32_e32 v9, v3
	v_mov_b32_e32 v11, v3
	s_mov_b32 s7, 0
	v_add_u32_e32 v129, v22, v19
	v_add_u32_e32 v130, v122, v20
	s_waitcnt vmcnt(0)
	v_lshlrev_b32_e32 v123, 10, v12
	v_lshlrev_b32_e32 v124, 10, v13
	v_lshlrev_b32_e32 v125, 10, v14
	v_or_b32_e32 v4, v123, v121
	v_lshlrev_b32_e32 v126, 10, v15
	v_or_b32_e32 v6, v124, v121
	v_or_b32_e32 v8, v125, v121
	v_lshl_add_u64 v[4:5], v[4:5], 1, s[28:29]
	v_or_b32_e32 v10, v126, v121
	v_lshl_add_u64 v[6:7], v[6:7], 1, s[28:29]
	v_lshl_add_u64 v[4:5], v[8:9], 1, s[28:29]
	v_lshl_add_u64 v[6:7], v[10:11], 1, s[28:29]
	v_lshl_add_u64 v[4:5], v[2:3], 1, s[44:45]
	v_add_co_u32_e32 v6, vcc, s40, v4
	v_and_b32_e32 v2, 1, v118
	s_nop 0
	v_addc_co_u32_e32 v7, vcc, 0, v5, vcc
	v_add_co_u32_e32 v6, vcc, s18, v4
	v_cmp_eq_u32_e64 s[46:47], 0, v2
	s_nop 0
	v_addc_co_u32_e32 v7, vcc, 0, v5, vcc
	v_add_co_u32_e32 v4, vcc, s19, v4
	v_bfe_i32 v2, v118, 2, 1
	s_nop 0
	v_addc_co_u32_e32 v5, vcc, 0, v5, vcc
	v_and_b32_e32 v2, 0x2040, v2
	v_and_b32_e32 v4, 0xffffffc0, v16
	v_add_u32_e32 v2, v2, v4
	v_lshlrev_b32_e32 v4, 4, v118
	v_and_b32_e32 v5, 48, v4
	v_or3_b32 v4, v21, s15, v18
	v_mul_lo_u32 v6, v17, s48
	v_lshlrev_b32_e32 v7, 4, v119
	v_add_u32_e32 v116, 0x30000, v4
	v_mov_b32_e32 v4, 0
	v_add_u32_e32 v127, v2, v5
	v_add_u32_e32 v128, v6, v7
	s_lshl_b32 s48, s6, 8
	v_lshrrev_b32_e32 v116, 6, v118
	v_lshlrev_b32_e32 v116, 4, v116
	v_bfe_u32 v117, v118, 4, 2
	v_add_u32_e32 v116, v116, v117
	v_mul_u32_u24_e32 v116, 0x800, v116
	v_add_u32_e32 v116, s48, v116
	v_bfe_u32 v68, v118, 1, 3
	v_xor_b32_e32 v68, v68, v117
	v_lshlrev_b32_e32 v68, 1, v68
	v_and_b32_e32 v117, 1, v118
	v_or_b32_e32 v68, v68, v117
	v_lshl_add_u32 v214, v68, 4, v116
	v_add_u32_e32 v215, 0x2000, v214
	v_xor_b32_e32 v68, 8, v68
	v_lshl_add_u32 v216, v68, 4, v116
	v_add_u32_e32 v216, 0x4000, v216
	v_add_u32_e32 v217, 0x2000, v216
	v_lshrrev_b32_e32 v116, 3, v118
	v_lshlrev_b32_e32 v116, 2, v116
	s_barrier
	ds_write_b32 v116, v123 offset:36864
	ds_write_b32 v116, v124 offset:36992
	ds_write_b32 v116, v125 offset:37120
	ds_write_b32 v116, v126 offset:37248
	s_waitcnt lgkmcnt(0)
	s_barrier
	v_lshrrev_b32_e32 v117, 6, v118
	v_lshlrev_b32_e32 v117, 5, v117
	v_bfe_u32 v68, v118, 2, 4
	v_add_u32_e32 v117, v117, v68
	v_lshlrev_b32_e32 v117, 2, v117
	ds_read_b32 v123, v117 offset:36864
	ds_read_b32 v125, v117 offset:36928
	v_bfe_u32 v68, v118, 4, 2
	v_sub_u32_e32 v68, 0, v68
	v_and_b32_e32 v68, 3, v68
	v_and_b32_e32 v116, 3, v118
	v_xor_b32_e32 v68, v68, v116
	v_lshlrev_b32_e32 v68, 4, v68
	s_waitcnt lgkmcnt(0)
	v_lshl_add_u32 v123, v123, 1, v68
	v_add_u32_e32 v124, 64, v123
	v_lshl_add_u32 v125, v125, 1, v68
	v_add_u32_e32 v126, 64, v125
	v_bfe_u32 v116, v118, 2, 2
	v_sub_u32_e32 v116, 0, v116
	v_and_b32_e32 v116, 3, v116
	v_lshlrev_b32_e32 v116, 4, v116
	v_xor_b32_e32 v129, v129, v116
	v_bfe_u32 v116, v118, 4, 2
	v_lshlrev_b32_e32 v116, 3, v116
	v_bfe_u32 v117, v118, 2, 2
	v_add_u32_e32 v116, v116, v117
	v_lshlrev_b32_e32 v116, 8, v116
	v_lshrrev_b32_e32 v68, 6, v118
	v_lshrrev_b32_e32 v127, 4, v118
	v_xor_b32_e32 v68, v68, v127
	v_and_b32_e32 v68, 1, v68
	v_lshlrev_b32_e32 v68, 7, v68
	v_or_b32_e32 v116, v116, v68
	v_and_b32_e32 v68, 3, v118
	v_lshlrev_b32_e32 v68, 3, v68
	v_or_b32_e32 v116, v116, v68
	v_xor_b32_e32 v68, 0, v117
	v_lshl_or_b32 v127, v68, 5, v116
	v_xor_b32_e32 v68, 1, v117
	v_lshl_or_b32 v128, v68, 5, v116
	v_xor_b32_e32 v68, 2, v117
	v_lshl_or_b32 v130, v68, 5, v116
	v_xor_b32_e32 v68, 3, v117
	v_lshl_or_b32 v122, v68, 5, v116
	v_lshrrev_b32_e32 v116, 6, v118
	s_nop 1
	v_readfirstlane_b32 s98, v116
	s_nop 1
	s_lshl_b32 s99, s98, 12
	s_lshl_b32 s98, s98, 11
	s_barrier
;     ...
;     gloadB(0, rb0); gloadA(0, ra0); gloadB(1, rb1);
;     for (int kt = 0; kt < nk; kt += 2) {
;         __syncthreads();
;         lstore(ra0, rb0);
;         __syncthreads();
;         gloadA(kt + 1, ra0);
;         if (kt + 2 < nk) gloadB(kt + 2, rb0);
;         compute();
;         __syncthreads();
;         lstore(ra0, rb1);
;         __syncthreads();
;         if (kt + 2 < nk) gloadA(kt + 2, ra0);
;         if (kt + 3 < nk) gloadB(kt + 3, rb1);
;         compute();
;     }
; __device__ __forceinline__ void ph_moe1_mfma(const Ctx& c, int layer, int tile, const int* sm, unsigned char* lds) {
;     ...
;     asm volatile("s_waitcnt vmcnt(0)" ::: "memory");
;     __syncthreads();
;     if (c.tid == 0) (void)__hip_atomic_fetch_add(flag, 1u, __ATOMIC_RELAXED, __HIP_MEMORY_SCOPE_AGENT);
	s_add_u32 m0, s98, 0x0
	s_nop 0
	global_load_lds_dwordx4 v123, s[28:29]
	s_add_u32 m0, s98, 0x2040
	s_nop 0
	global_load_lds_dwordx4 v124, s[28:29]
	s_add_u32 m0, s98, 0x400
	s_nop 0
	global_load_lds_dwordx4 v125, s[28:29]
	s_add_u32 m0, s98, 0x2440
	s_nop 0
	global_load_lds_dwordx4 v126, s[28:29]
	s_add_u32 m0, s99, 0x4080
	s_nop 0
	global_load_lds_dwordx4 v214, s[44:45]
	s_add_u32 m0, s99, 0x4480
	s_nop 0
	global_load_lds_dwordx4 v215, s[44:45]
	s_add_u32 m0, s99, 0x4880
	s_nop 0
	global_load_lds_dwordx4 v216, s[44:45]
	s_add_u32 m0, s99, 0x4c80
	s_nop 0
	global_load_lds_dwordx4 v217, s[44:45]
	s_add_u32 s28, s28, 0x80
	s_addc_u32 s29, s29, 0
	s_add_u32 s44, s44, 0x20000
	s_addc_u32 s45, s45, 0
	s_mov_b32 s7, 0
	v_mov_b32_e32 v5, v4
	v_mov_b32_e32 v6, v4
	v_mov_b32_e32 v7, v4
	v_mov_b32_e32 v16, v4
	v_mov_b32_e32 v17, v4
	v_mov_b32_e32 v18, v4
	v_mov_b32_e32 v19, v4
	v_mov_b32_e32 v8, v4
	v_mov_b32_e32 v9, v4
	v_mov_b32_e32 v10, v4
	v_mov_b32_e32 v11, v4
	v_mov_b32_e32 v12, v4
	v_mov_b32_e32 v13, v4
	v_mov_b32_e32 v14, v4
	v_mov_b32_e32 v15, v4
	v_mov_b32_e32 v20, v4
	v_mov_b32_e32 v21, v4
	v_mov_b32_e32 v22, v4
	v_mov_b32_e32 v23, v4
	v_mov_b32_e32 v60, v4
	v_mov_b32_e32 v61, v4
	v_mov_b32_e32 v62, v4
	v_mov_b32_e32 v63, v4
	v_mov_b32_e32 v28, v4
	v_mov_b32_e32 v29, v4
	v_mov_b32_e32 v30, v4
	v_mov_b32_e32 v31, v4
	v_mov_b32_e32 v72, v4
	v_mov_b32_e32 v73, v4
	v_mov_b32_e32 v74, v4
	v_mov_b32_e32 v75, v4
	v_mov_b32_e32 v84, v4
	v_mov_b32_e32 v85, v4
	v_mov_b32_e32 v86, v4
	v_mov_b32_e32 v87, v4
	v_mov_b32_e32 v92, v4
	v_mov_b32_e32 v93, v4
	v_mov_b32_e32 v94, v4
	v_mov_b32_e32 v95, v4
	v_mov_b32_e32 v88, v4
	v_mov_b32_e32 v89, v4
	v_mov_b32_e32 v90, v4
	v_mov_b32_e32 v91, v4
	v_mov_b32_e32 v96, v4
	v_mov_b32_e32 v97, v4
	v_mov_b32_e32 v98, v4
	v_mov_b32_e32 v99, v4
	v_mov_b32_e32 v100, v4
	v_mov_b32_e32 v101, v4
	v_mov_b32_e32 v102, v4
	v_mov_b32_e32 v103, v4
	v_mov_b32_e32 v108, v4
	v_mov_b32_e32 v109, v4
	v_mov_b32_e32 v110, v4
	v_mov_b32_e32 v111, v4
	v_mov_b32_e32 v104, v4
	v_mov_b32_e32 v105, v4
	v_mov_b32_e32 v106, v4
	v_mov_b32_e32 v107, v4
	v_mov_b32_e32 v112, v4
	v_mov_b32_e32 v113, v4
	v_mov_b32_e32 v114, v4
	v_mov_b32_e32 v115, v4
	s_waitcnt vmcnt(0)
	s_barrier
	s_cmp_eq_u32 s101, 0
	s_cbranch_scc1 .Lm1_nopend1
	s_lshl_b32 s50, s100, 2
	s_add_u32 s50, s42, s50
	s_addc_u32 s51, s43, 0
	v_cmp_eq_u32_e32 vcc, 0, v118
	s_and_saveexec_b64 s[48:49], vcc
	v_mov_b32_e32 v68, 1
	global_atomic_add v221, v68, s[50:51]
	s_mov_b64 exec, s[48:49]
	s_mov_b32 s101, 0
.Lm1_nopend1:
.Lm1_loop:
	s_add_u32 m0, s98, 0x9000
	ds_read_b64_tr_b16 v[174:175], v127 offset:16512
	ds_read_b64_tr_b16 v[176:177], v127 offset:17536
	ds_read_b128 v[158:161], v129
	ds_read_b64_tr_b16 v[178:179], v128 offset:16512
	ds_read_b64_tr_b16 v[180:181], v128 offset:17536
	s_waitcnt lgkmcnt(2)
	v_mfma_f32_16x16x32_bf16 v[112:115], v[174:177], v[158:161], v[112:115]
	global_load_lds_dwordx4 v123, s[28:29]
	s_add_u32 m0, s98, 0xb040
	ds_read_b64_tr_b16 v[182:183], v130 offset:16512
	ds_read_b64_tr_b16 v[184:185], v130 offset:17536
	s_waitcnt lgkmcnt(2)
	v_mfma_f32_16x16x32_bf16 v[104:107], v[178:181], v[158:161], v[104:107]
	global_load_lds_dwordx4 v124, s[28:29]
	s_add_u32 m0, s98, 0x9400
	ds_read_b64_tr_b16 v[186:187], v122 offset:16512
	ds_read_b64_tr_b16 v[188:189], v122 offset:17536
	s_waitcnt lgkmcnt(2)
	v_mfma_f32_16x16x32_bf16 v[108:111], v[182:185], v[158:161], v[108:111]
	global_load_lds_dwordx4 v125, s[28:29]
	s_add_u32 m0, s98, 0xb440
	ds_read_b128 v[162:165], v129 offset:1024
	s_waitcnt lgkmcnt(1)
	v_mfma_f32_16x16x32_bf16 v[100:103], v[186:189], v[158:161], v[100:103]
	global_load_lds_dwordx4 v126, s[28:29]
	s_add_u32 m0, s99, 0xd080
	ds_read_b128 v[166:169], v129 offset:2048
	s_waitcnt lgkmcnt(1)
	v_mfma_f32_16x16x32_bf16 v[96:99], v[174:177], v[162:165], v[96:99]
	global_load_lds_dwordx4 v214, s[44:45]
	s_add_u32 m0, s99, 0xd480
	ds_read_b128 v[170:173], v129 offset:3072
	v_mfma_f32_16x16x32_bf16 v[88:91], v[178:181], v[162:165], v[88:91]
	global_load_lds_dwordx4 v215, s[44:45]
	s_add_u32 m0, s99, 0xd880
	ds_read_b64_tr_b16 v[190:191], v127 offset:24704
	ds_read_b64_tr_b16 v[192:193], v127 offset:25728
	v_mfma_f32_16x16x32_bf16 v[92:95], v[182:185], v[162:165], v[92:95]
	global_load_lds_dwordx4 v216, s[44:45]
	s_add_u32 m0, s99, 0xdc80
	ds_read_b64_tr_b16 v[132:133], v128 offset:24704
	ds_read_b64_tr_b16 v[134:135], v128 offset:25728
	v_mfma_f32_16x16x32_bf16 v[84:87], v[186:189], v[162:165], v[84:87]
	global_load_lds_dwordx4 v217, s[44:45]
	s_add_u32 s28, s28, 0x80
	s_addc_u32 s29, s29, 0
	s_add_u32 s44, s44, 0x20000
	s_addc_u32 s45, s45, 0
	ds_read_b128 v[158:161], v129 offset:8256
	s_waitcnt lgkmcnt(6)
	v_mfma_f32_16x16x32_bf16 v[72:75], v[174:177], v[166:169], v[72:75]
	ds_read_b64_tr_b16 v[136:137], v130 offset:24704
	ds_read_b64_tr_b16 v[138:139], v130 offset:25728
	v_mfma_f32_16x16x32_bf16 v[28:31], v[178:181], v[166:169], v[28:31]
	ds_read_b64_tr_b16 v[140:141], v122 offset:24704
	ds_read_b64_tr_b16 v[142:143], v122 offset:25728
	v_mfma_f32_16x16x32_bf16 v[60:63], v[182:185], v[166:169], v[60:63]
	v_mfma_f32_16x16x32_bf16 v[20:23], v[186:189], v[166:169], v[20:23]
	ds_read_b128 v[162:165], v129 offset:9280
	s_waitcnt lgkmcnt(10)
	v_mfma_f32_16x16x32_bf16 v[12:15], v[174:177], v[170:173], v[12:15]
	v_mfma_f32_16x16x32_bf16 v[8:11], v[178:181], v[170:173], v[8:11]
	v_mfma_f32_16x16x32_bf16 v[16:19], v[182:185], v[170:173], v[16:19]
	v_mfma_f32_16x16x32_bf16 v[4:7], v[186:189], v[170:173], v[4:7]
	ds_read_b128 v[166:169], v129 offset:10304
	s_waitcnt lgkmcnt(6)
	v_mfma_f32_16x16x32_bf16 v[112:115], v[190:193], v[158:161], v[112:115]
	v_mfma_f32_16x16x32_bf16 v[104:107], v[132:135], v[158:161], v[104:107]
	s_waitcnt lgkmcnt(4)
	v_mfma_f32_16x16x32_bf16 v[108:111], v[136:139], v[158:161], v[108:111]
	s_waitcnt lgkmcnt(2)
	v_mfma_f32_16x16x32_bf16 v[100:103], v[140:143], v[158:161], v[100:103]
	ds_read_b128 v[170:173], v129 offset:11328
	s_waitcnt lgkmcnt(2)
	v_mfma_f32_16x16x32_bf16 v[96:99], v[190:193], v[162:165], v[96:99]
	v_mfma_f32_16x16x32_bf16 v[88:91], v[132:135], v[162:165], v[88:91]
	v_mfma_f32_16x16x32_bf16 v[92:95], v[136:139], v[162:165], v[92:95]
	v_mfma_f32_16x16x32_bf16 v[84:87], v[140:143], v[162:165], v[84:87]
	s_waitcnt lgkmcnt(1)
	v_mfma_f32_16x16x32_bf16 v[72:75], v[190:193], v[166:169], v[72:75]
	v_mfma_f32_16x16x32_bf16 v[28:31], v[132:135], v[166:169], v[28:31]
	v_mfma_f32_16x16x32_bf16 v[60:63], v[136:139], v[166:169], v[60:63]
	v_mfma_f32_16x16x32_bf16 v[20:23], v[140:143], v[166:169], v[20:23]
	s_waitcnt lgkmcnt(0)
	v_mfma_f32_16x16x32_bf16 v[12:15], v[190:193], v[170:173], v[12:15]
	v_mfma_f32_16x16x32_bf16 v[8:11], v[132:135], v[170:173], v[8:11]
	v_mfma_f32_16x16x32_bf16 v[16:19], v[136:139], v[170:173], v[16:19]
	v_mfma_f32_16x16x32_bf16 v[4:7], v[140:143], v[170:173], v[4:7]
	s_waitcnt vmcnt(0) lgkmcnt(0)
	s_barrier
; #define LAS __attribute__((address_space(3)))
; __device__ __forceinline__ s16x4 lds_tr(lds_cptr p) { return __builtin_bit_cast(s16x4, __builtin_amdgcn_ds_read_tr16_b64_v4i16((LAS s16x4*)p)); }
;     ...
;     auto compute = [&]() __attribute__((always_inline)) {
; #pragma unroll
;         for (int kh = 0; kh < 2; ++kh) {
;             bf16x8 af[4], bfr[4];
; #pragma unroll
;             for (int m = 0; m < 4; ++m) af[m] = *(const LAS bf16x8*)(la + kh * GA_KH + m * 1024);
; #pragma unroll
;             for (int n = 0; n < 4; ++n) {
;                 const s16x4 r0 = lds_tr(lb + kh * 32 * GB_ST + n * 32), r1 = lds_tr(lb + kh * 32 * GB_ST + n * 32 + bsw);
;                 bfr[n] = (bf16x8){r0[0], r0[1], r0[2], r0[3], r1[0], r1[1], r1[2], r1[3]};
;             }
; #pragma unroll
;             for (int m = 0; m < 4; ++m)
; #pragma unroll
;                 for (int n = 0; n < 4; ++n) acc[m][n] = __builtin_amdgcn_mfma_f32_16x16x32_bf16(bfr[n], af[m], acc[m][n], 0, 0, 0);
;         }
;     };
;     ...
;     gloadB(0, rb0); gloadA(0, ra0); gloadB(1, rb1);
;     for (int kt = 0; kt < nk; kt += 2) {
;         __syncthreads();
;         lstore(ra0, rb0);
;         __syncthreads();
;         gloadA(kt + 1, ra0);
;         if (kt + 2 < nk) gloadB(kt + 2, rb0);
;         compute();
;         __syncthreads();
;         lstore(ra0, rb1);
;         __syncthreads();
;         if (kt + 2 < nk) gloadA(kt + 2, ra0);
;         if (kt + 3 < nk) gloadB(kt + 3, rb1);
;         compute();
;     }
	s_add_u32 m0, s98, 0x0
	ds_read_b64_tr_b16 v[174:175], v127 offset:53376
	ds_read_b64_tr_b16 v[176:177], v127 offset:54400
	ds_read_b128 v[158:161], v129 offset:36864
	ds_read_b64_tr_b16 v[178:179], v128 offset:53376
	ds_read_b64_tr_b16 v[180:181], v128 offset:54400
	s_waitcnt lgkmcnt(2)
	v_mfma_f32_16x16x32_bf16 v[112:115], v[174:177], v[158:161], v[112:115]
	global_load_lds_dwordx4 v123, s[28:29]
	s_add_u32 m0, s98, 0x2040
	ds_read_b64_tr_b16 v[182:183], v130 offset:53376
	ds_read_b64_tr_b16 v[184:185], v130 offset:54400
	s_waitcnt lgkmcnt(2)
	v_mfma_f32_16x16x32_bf16 v[104:107], v[178:181], v[158:161], v[104:107]
	global_load_lds_dwordx4 v124, s[28:29]
	s_add_u32 m0, s98, 0x400
	ds_read_b64_tr_b16 v[186:187], v122 offset:53376
	ds_read_b64_tr_b16 v[188:189], v122 offset:54400
	s_waitcnt lgkmcnt(2)
	v_mfma_f32_16x16x32_bf16 v[108:111], v[182:185], v[158:161], v[108:111]
	global_load_lds_dwordx4 v125, s[28:29]
	s_add_u32 m0, s98, 0x2440
	ds_read_b128 v[162:165], v129 offset:37888
	s_waitcnt lgkmcnt(1)
	v_mfma_f32_16x16x32_bf16 v[100:103], v[186:189], v[158:161], v[100:103]
	global_load_lds_dwordx4 v126, s[28:29]
	s_add_u32 m0, s99, 0x4080
	ds_read_b128 v[166:169], v129 offset:38912
	s_waitcnt lgkmcnt(1)
	v_mfma_f32_16x16x32_bf16 v[96:99], v[174:177], v[162:165], v[96:99]
	global_load_lds_dwordx4 v214, s[44:45]
	s_add_u32 m0, s99, 0x4480
	ds_read_b128 v[170:173], v129 offset:39936
	v_mfma_f32_16x16x32_bf16 v[88:91], v[178:181], v[162:165], v[88:91]
	global_load_lds_dwordx4 v215, s[44:45]
	s_add_u32 m0, s99, 0x4880
	ds_read_b64_tr_b16 v[190:191], v127 offset:61568
	ds_read_b64_tr_b16 v[192:193], v127 offset:62592
	v_mfma_f32_16x16x32_bf16 v[92:95], v[182:185], v[162:165], v[92:95]
	global_load_lds_dwordx4 v216, s[44:45]
	s_add_u32 m0, s99, 0x4c80
	ds_read_b64_tr_b16 v[132:133], v128 offset:61568
	ds_read_b64_tr_b16 v[134:135], v128 offset:62592
	v_mfma_f32_16x16x32_bf16 v[84:87], v[186:189], v[162:165], v[84:87]
	global_load_lds_dwordx4 v217, s[44:45]
	s_add_u32 s28, s28, 0x80
	s_addc_u32 s29, s29, 0
	s_add_u32 s44, s44, 0x20000
	s_addc_u32 s45, s45, 0
	ds_read_b128 v[158:161], v129 offset:45120
	s_waitcnt lgkmcnt(6)
	v_mfma_f32_16x16x32_bf16 v[72:75], v[174:177], v[166:169], v[72:75]
	ds_read_b64_tr_b16 v[136:137], v130 offset:61568
	ds_read_b64_tr_b16 v[138:139], v130 offset:62592
	v_mfma_f32_16x16x32_bf16 v[28:31], v[178:181], v[166:169], v[28:31]
	ds_read_b64_tr_b16 v[140:141], v122 offset:61568
	ds_read_b64_tr_b16 v[142:143], v122 offset:62592
	v_mfma_f32_16x16x32_bf16 v[60:63], v[182:185], v[166:169], v[60:63]
	v_mfma_f32_16x16x32_bf16 v[20:23], v[186:189], v[166:169], v[20:23]
	ds_read_b128 v[162:165], v129 offset:46144
	s_waitcnt lgkmcnt(10)
	v_mfma_f32_16x16x32_bf16 v[12:15], v[174:177], v[170:173], v[12:15]
	v_mfma_f32_16x16x32_bf16 v[8:11], v[178:181], v[170:173], v[8:11]
	v_mfma_f32_16x16x32_bf16 v[16:19], v[182:185], v[170:173], v[16:19]
	v_mfma_f32_16x16x32_bf16 v[4:7], v[186:189], v[170:173], v[4:7]
	ds_read_b128 v[166:169], v129 offset:47168
	s_waitcnt lgkmcnt(6)
	v_mfma_f32_16x16x32_bf16 v[112:115], v[190:193], v[158:161], v[112:115]
	v_mfma_f32_16x16x32_bf16 v[104:107], v[132:135], v[158:161], v[104:107]
	s_waitcnt lgkmcnt(4)
	v_mfma_f32_16x16x32_bf16 v[108:111], v[136:139], v[158:161], v[108:111]
	s_waitcnt lgkmcnt(2)
	v_mfma_f32_16x16x32_bf16 v[100:103], v[140:143], v[158:161], v[100:103]
	ds_read_b128 v[170:173], v129 offset:48192
	s_waitcnt lgkmcnt(2)
	v_mfma_f32_16x16x32_bf16 v[96:99], v[190:193], v[162:165], v[96:99]
	v_mfma_f32_16x16x32_bf16 v[88:91], v[132:135], v[162:165], v[88:91]
	v_mfma_f32_16x16x32_bf16 v[92:95], v[136:139], v[162:165], v[92:95]
	v_mfma_f32_16x16x32_bf16 v[84:87], v[140:143], v[162:165], v[84:87]
	s_waitcnt lgkmcnt(1)
	v_mfma_f32_16x16x32_bf16 v[72:75], v[190:193], v[166:169], v[72:75]
	v_mfma_f32_16x16x32_bf16 v[28:31], v[132:135], v[166:169], v[28:31]
	v_mfma_f32_16x16x32_bf16 v[60:63], v[136:139], v[166:169], v[60:63]
	v_mfma_f32_16x16x32_bf16 v[20:23], v[140:143], v[166:169], v[20:23]
	s_waitcnt lgkmcnt(0)
	v_mfma_f32_16x16x32_bf16 v[12:15], v[190:193], v[170:173], v[12:15]
	v_mfma_f32_16x16x32_bf16 v[8:11], v[132:135], v[170:173], v[8:11]
	v_mfma_f32_16x16x32_bf16 v[16:19], v[136:139], v[170:173], v[16:19]
	v_mfma_f32_16x16x32_bf16 v[4:7], v[140:143], v[170:173], v[4:7]
	s_waitcnt vmcnt(0) lgkmcnt(0)
	s_barrier
	s_add_i32 s7, s7, 2
	s_cmp_lt_u32 s7, 14
	s_cbranch_scc1 .Lm1_loop
; #define LAS __attribute__((address_space(3)))
; __device__ __forceinline__ s16x4 lds_tr(lds_cptr p) { return __builtin_bit_cast(s16x4, __builtin_amdgcn_ds_read_tr16_b64_v4i16((LAS s16x4*)p)); }
;     ...
;     auto compute = [&]() __attribute__((always_inline)) {
; #pragma unroll
;         for (int kh = 0; kh < 2; ++kh) {
;             bf16x8 af[4], bfr[4];
; #pragma unroll
;             for (int m = 0; m < 4; ++m) af[m] = *(const LAS bf16x8*)(la + kh * GA_KH + m * 1024);
; #pragma unroll
;             for (int n = 0; n < 4; ++n) {
;                 const s16x4 r0 = lds_tr(lb + kh * 32 * GB_ST + n * 32), r1 = lds_tr(lb + kh * 32 * GB_ST + n * 32 + bsw);
;                 bfr[n] = (bf16x8){r0[0], r0[1], r0[2], r0[3], r1[0], r1[1], r1[2], r1[3]};
;             }
; #pragma unroll
;             for (int m = 0; m < 4; ++m)
; #pragma unroll
;                 for (int n = 0; n < 4; ++n) acc[m][n] = __builtin_amdgcn_mfma_f32_16x16x32_bf16(bfr[n], af[m], acc[m][n], 0, 0, 0);
;         }
;     };
;     ...
;     gloadB(0, rb0); gloadA(0, ra0); gloadB(1, rb1);
;     for (int kt = 0; kt < nk; kt += 2) {
;         __syncthreads();
;         lstore(ra0, rb0);
;         __syncthreads();
;         gloadA(kt + 1, ra0);
;         if (kt + 2 < nk) gloadB(kt + 2, rb0);
;         compute();
;         __syncthreads();
;         lstore(ra0, rb1);
;         __syncthreads();
;         if (kt + 2 < nk) gloadA(kt + 2, ra0);
;         if (kt + 3 < nk) gloadB(kt + 3, rb1);
;         compute();
;     }
	s_add_u32 m0, s98, 0x9000
	ds_read_b64_tr_b16 v[174:175], v127 offset:16512
	ds_read_b64_tr_b16 v[176:177], v127 offset:17536
	ds_read_b128 v[158:161], v129
	ds_read_b64_tr_b16 v[178:179], v128 offset:16512
	ds_read_b64_tr_b16 v[180:181], v128 offset:17536
	s_waitcnt lgkmcnt(2)
	v_mfma_f32_16x16x32_bf16 v[112:115], v[174:177], v[158:161], v[112:115]
	global_load_lds_dwordx4 v123, s[28:29]
	s_add_u32 m0, s98, 0xb040
	ds_read_b64_tr_b16 v[182:183], v130 offset:16512
	ds_read_b64_tr_b16 v[184:185], v130 offset:17536
	s_waitcnt lgkmcnt(2)
	v_mfma_f32_16x16x32_bf16 v[104:107], v[178:181], v[158:161], v[104:107]
	global_load_lds_dwordx4 v124, s[28:29]
	s_add_u32 m0, s98, 0x9400
	ds_read_b64_tr_b16 v[186:187], v122 offset:16512
	ds_read_b64_tr_b16 v[188:189], v122 offset:17536
	s_waitcnt lgkmcnt(2)
	v_mfma_f32_16x16x32_bf16 v[108:111], v[182:185], v[158:161], v[108:111]
	global_load_lds_dwordx4 v125, s[28:29]
	s_add_u32 m0, s98, 0xb440
	ds_read_b128 v[162:165], v129 offset:1024
	s_waitcnt lgkmcnt(1)
	v_mfma_f32_16x16x32_bf16 v[100:103], v[186:189], v[158:161], v[100:103]
	global_load_lds_dwordx4 v126, s[28:29]
	s_add_u32 m0, s99, 0xd080
	ds_read_b128 v[166:169], v129 offset:2048
	s_waitcnt lgkmcnt(1)
	v_mfma_f32_16x16x32_bf16 v[96:99], v[174:177], v[162:165], v[96:99]
	global_load_lds_dwordx4 v214, s[44:45]
	s_add_u32 m0, s99, 0xd480
	ds_read_b128 v[170:173], v129 offset:3072
	v_mfma_f32_16x16x32_bf16 v[88:91], v[178:181], v[162:165], v[88:91]
	global_load_lds_dwordx4 v215, s[44:45]
	s_add_u32 m0, s99, 0xd880
	ds_read_b64_tr_b16 v[190:191], v127 offset:24704
	ds_read_b64_tr_b16 v[192:193], v127 offset:25728
	v_mfma_f32_16x16x32_bf16 v[92:95], v[182:185], v[162:165], v[92:95]
	global_load_lds_dwordx4 v216, s[44:45]
	s_add_u32 m0, s99, 0xdc80
	ds_read_b64_tr_b16 v[132:133], v128 offset:24704
	ds_read_b64_tr_b16 v[134:135], v128 offset:25728
	v_mfma_f32_16x16x32_bf16 v[84:87], v[186:189], v[162:165], v[84:87]
	global_load_lds_dwordx4 v217, s[44:45]
	s_add_u32 s28, s28, 0x80
	s_addc_u32 s29, s29, 0
	s_add_u32 s44, s44, 0x20000
	s_addc_u32 s45, s45, 0
	ds_read_b128 v[158:161], v129 offset:8256
	s_waitcnt lgkmcnt(6)
	v_mfma_f32_16x16x32_bf16 v[72:75], v[174:177], v[166:169], v[72:75]
	ds_read_b64_tr_b16 v[136:137], v130 offset:24704
	ds_read_b64_tr_b16 v[138:139], v130 offset:25728
	v_mfma_f32_16x16x32_bf16 v[28:31], v[178:181], v[166:169], v[28:31]
	ds_read_b64_tr_b16 v[140:141], v122 offset:24704
	ds_read_b64_tr_b16 v[142:143], v122 offset:25728
	v_mfma_f32_16x16x32_bf16 v[60:63], v[182:185], v[166:169], v[60:63]
	v_mfma_f32_16x16x32_bf16 v[20:23], v[186:189], v[166:169], v[20:23]
	ds_read_b128 v[162:165], v129 offset:9280
	s_waitcnt lgkmcnt(10)
	v_mfma_f32_16x16x32_bf16 v[12:15], v[174:177], v[170:173], v[12:15]
	v_mfma_f32_16x16x32_bf16 v[8:11], v[178:181], v[170:173], v[8:11]
	v_mfma_f32_16x16x32_bf16 v[16:19], v[182:185], v[170:173], v[16:19]
	v_mfma_f32_16x16x32_bf16 v[4:7], v[186:189], v[170:173], v[4:7]
	ds_read_b128 v[166:169], v129 offset:10304
	s_waitcnt lgkmcnt(6)
	v_mfma_f32_16x16x32_bf16 v[112:115], v[190:193], v[158:161], v[112:115]
	v_mfma_f32_16x16x32_bf16 v[104:107], v[132:135], v[158:161], v[104:107]
	s_waitcnt lgkmcnt(4)
	v_mfma_f32_16x16x32_bf16 v[108:111], v[136:139], v[158:161], v[108:111]
	s_waitcnt lgkmcnt(2)
	v_mfma_f32_16x16x32_bf16 v[100:103], v[140:143], v[158:161], v[100:103]
	ds_read_b128 v[170:173], v129 offset:11328
	s_waitcnt lgkmcnt(2)
	v_mfma_f32_16x16x32_bf16 v[96:99], v[190:193], v[162:165], v[96:99]
	v_mfma_f32_16x16x32_bf16 v[88:91], v[132:135], v[162:165], v[88:91]
	v_mfma_f32_16x16x32_bf16 v[92:95], v[136:139], v[162:165], v[92:95]
	v_mfma_f32_16x16x32_bf16 v[84:87], v[140:143], v[162:165], v[84:87]
	s_waitcnt lgkmcnt(1)
	v_mfma_f32_16x16x32_bf16 v[72:75], v[190:193], v[166:169], v[72:75]
	v_mfma_f32_16x16x32_bf16 v[28:31], v[132:135], v[166:169], v[28:31]
	v_mfma_f32_16x16x32_bf16 v[60:63], v[136:139], v[166:169], v[60:63]
	v_mfma_f32_16x16x32_bf16 v[20:23], v[140:143], v[166:169], v[20:23]
	s_waitcnt lgkmcnt(0)
	v_mfma_f32_16x16x32_bf16 v[12:15], v[190:193], v[170:173], v[12:15]
	v_mfma_f32_16x16x32_bf16 v[8:11], v[132:135], v[170:173], v[8:11]
	v_mfma_f32_16x16x32_bf16 v[16:19], v[136:139], v[170:173], v[16:19]
	v_mfma_f32_16x16x32_bf16 v[4:7], v[140:143], v[170:173], v[4:7]
	s_waitcnt vmcnt(0) lgkmcnt(0)
	s_barrier
; #define LAS __attribute__((address_space(3)))
; __device__ __forceinline__ float silu_f(float x) { return x * __builtin_amdgcn_rcpf(1.f + __expf(-x)); }
; __device__ __forceinline__ unsigned pk2bf(float lo, float hi) { const f32x2 v = {lo, hi}; return __builtin_bit_cast(unsigned, __builtin_convertvector(v, bf16x2_t)); }
;     template <class T> __device__ __forceinline__ T* w(size_t off) const { return (T*)(p->ws + off); }
; __device__ __forceinline__ s16x4 lds_tr(lds_cptr p) { return __builtin_bit_cast(s16x4, __builtin_amdgcn_ds_read_tr16_b64_v4i16((LAS s16x4*)p)); }
;     ...
;     auto compute = [&]() __attribute__((always_inline)) {
; #pragma unroll
;         for (int kh = 0; kh < 2; ++kh) {
;             bf16x8 af[4], bfr[4];
; #pragma unroll
;             for (int m = 0; m < 4; ++m) af[m] = *(const LAS bf16x8*)(la + kh * GA_KH + m * 1024);
; #pragma unroll
;             for (int n = 0; n < 4; ++n) {
;                 const s16x4 r0 = lds_tr(lb + kh * 32 * GB_ST + n * 32), r1 = lds_tr(lb + kh * 32 * GB_ST + n * 32 + bsw);
;                 bfr[n] = (bf16x8){r0[0], r0[1], r0[2], r0[3], r1[0], r1[1], r1[2], r1[3]};
;             }
; #pragma unroll
;             for (int m = 0; m < 4; ++m)
; #pragma unroll
;                 for (int n = 0; n < 4; ++n) acc[m][n] = __builtin_amdgcn_mfma_f32_16x16x32_bf16(bfr[n], af[m], acc[m][n], 0, 0, 0);
;         }
;     };
; __device__ __forceinline__ void ph_moe1_mfma(const Ctx& c, int layer, int tile, const int* sm, unsigned char* lds) {
;     ...
;     EPI_COORDS;
;     bf16* ACT = c.w<bf16>(WS_ACT);
; #pragma unroll
;     for (int m = 0; m < 4; ++m) {
;         const int rl = wr * 64 + m * 16 + fr;
; #pragma unroll
;         for (int n = 0; n < 2; ++n) {
;             const int col = nt * 64 + wc * 32 + n * 16 + fq * 4;
;             const f32x4 g = acc[m][n], u = acc[m][n + 2];
;             uint2 o; o.x = pk2bf(silu_f(g[0]) * u[0], silu_f(g[1]) * u[1]); o.y = pk2bf(silu_f(g[2]) * u[2], silu_f(g[3]) * u[3]);
;             __hip_atomic_store((unsigned long long*)(ACT + (size_t)(s0 + rl) * DE + col), ((unsigned long long)o.y << 32) | o.x, __ATOMIC_RELAXED, __HIP_MEMORY_SCOPE_AGENT);
	ds_read_b64_tr_b16 v[174:175], v127 offset:53376
	ds_read_b64_tr_b16 v[176:177], v127 offset:54400
	ds_read_b128 v[158:161], v129 offset:36864
	ds_read_b64_tr_b16 v[178:179], v128 offset:53376
	ds_read_b64_tr_b16 v[180:181], v128 offset:54400
	s_waitcnt lgkmcnt(2)
	v_mfma_f32_16x16x32_bf16 v[112:115], v[174:177], v[158:161], v[112:115]
	ds_read_b64_tr_b16 v[182:183], v130 offset:53376
	ds_read_b64_tr_b16 v[184:185], v130 offset:54400
	s_waitcnt lgkmcnt(2)
	v_mfma_f32_16x16x32_bf16 v[104:107], v[178:181], v[158:161], v[104:107]
	ds_read_b64_tr_b16 v[186:187], v122 offset:53376
	ds_read_b64_tr_b16 v[188:189], v122 offset:54400
	s_waitcnt lgkmcnt(2)
	v_mfma_f32_16x16x32_bf16 v[108:111], v[182:185], v[158:161], v[108:111]
	ds_read_b128 v[162:165], v129 offset:37888
	s_waitcnt lgkmcnt(1)
	v_mfma_f32_16x16x32_bf16 v[100:103], v[186:189], v[158:161], v[100:103]
	ds_read_b128 v[166:169], v129 offset:38912
	s_waitcnt lgkmcnt(1)
	v_mfma_f32_16x16x32_bf16 v[96:99], v[174:177], v[162:165], v[96:99]
	ds_read_b128 v[170:173], v129 offset:39936
	v_mfma_f32_16x16x32_bf16 v[88:91], v[178:181], v[162:165], v[88:91]
	ds_read_b64_tr_b16 v[190:191], v127 offset:61568
	ds_read_b64_tr_b16 v[192:193], v127 offset:62592
	v_mfma_f32_16x16x32_bf16 v[92:95], v[182:185], v[162:165], v[92:95]
	ds_read_b64_tr_b16 v[132:133], v128 offset:61568
	ds_read_b64_tr_b16 v[134:135], v128 offset:62592
	v_mfma_f32_16x16x32_bf16 v[84:87], v[186:189], v[162:165], v[84:87]
	ds_read_b128 v[158:161], v129 offset:45120
	s_waitcnt lgkmcnt(6)
	v_mfma_f32_16x16x32_bf16 v[72:75], v[174:177], v[166:169], v[72:75]
	ds_read_b64_tr_b16 v[136:137], v130 offset:61568
	ds_read_b64_tr_b16 v[138:139], v130 offset:62592
	v_mfma_f32_16x16x32_bf16 v[28:31], v[178:181], v[166:169], v[28:31]
	ds_read_b64_tr_b16 v[140:141], v122 offset:61568
	ds_read_b64_tr_b16 v[142:143], v122 offset:62592
	v_mfma_f32_16x16x32_bf16 v[60:63], v[182:185], v[166:169], v[60:63]
	v_mfma_f32_16x16x32_bf16 v[20:23], v[186:189], v[166:169], v[20:23]
	ds_read_b128 v[162:165], v129 offset:46144
	s_waitcnt lgkmcnt(10)
	v_mfma_f32_16x16x32_bf16 v[12:15], v[174:177], v[170:173], v[12:15]
	v_mfma_f32_16x16x32_bf16 v[8:11], v[178:181], v[170:173], v[8:11]
	v_mfma_f32_16x16x32_bf16 v[16:19], v[182:185], v[170:173], v[16:19]
	v_mfma_f32_16x16x32_bf16 v[4:7], v[186:189], v[170:173], v[4:7]
	ds_read_b128 v[166:169], v129 offset:47168
	s_waitcnt lgkmcnt(6)
	v_mfma_f32_16x16x32_bf16 v[112:115], v[190:193], v[158:161], v[112:115]
	v_mfma_f32_16x16x32_bf16 v[104:107], v[132:135], v[158:161], v[104:107]
	s_waitcnt lgkmcnt(4)
	v_mfma_f32_16x16x32_bf16 v[108:111], v[136:139], v[158:161], v[108:111]
	s_waitcnt lgkmcnt(2)
	v_mfma_f32_16x16x32_bf16 v[100:103], v[140:143], v[158:161], v[100:103]
	ds_read_b128 v[170:173], v129 offset:48192
	s_waitcnt lgkmcnt(2)
	v_mfma_f32_16x16x32_bf16 v[96:99], v[190:193], v[162:165], v[96:99]
	v_mfma_f32_16x16x32_bf16 v[88:91], v[132:135], v[162:165], v[88:91]
	v_mfma_f32_16x16x32_bf16 v[92:95], v[136:139], v[162:165], v[92:95]
	v_mfma_f32_16x16x32_bf16 v[84:87], v[140:143], v[162:165], v[84:87]
	s_waitcnt lgkmcnt(1)
	v_mfma_f32_16x16x32_bf16 v[72:75], v[190:193], v[166:169], v[72:75]
	v_mfma_f32_16x16x32_bf16 v[28:31], v[132:135], v[166:169], v[28:31]
	v_mfma_f32_16x16x32_bf16 v[60:63], v[136:139], v[166:169], v[60:63]
	v_mfma_f32_16x16x32_bf16 v[20:23], v[140:143], v[166:169], v[20:23]
	s_waitcnt lgkmcnt(0)
	v_mfma_f32_16x16x32_bf16 v[12:15], v[190:193], v[170:173], v[12:15]
	v_mfma_f32_16x16x32_bf16 v[8:11], v[132:135], v[170:173], v[8:11]
	v_mfma_f32_16x16x32_bf16 v[16:19], v[136:139], v[170:173], v[16:19]
	v_mfma_f32_16x16x32_bf16 v[4:7], v[140:143], v[170:173], v[4:7]
	s_waitcnt vmcnt(0) lgkmcnt(0)
	s_barrier
.LBB0_170:
	s_add_u32 s28, s42, 0xb3c6000
	v_lshrrev_b32_e32 v2, 1, v118
	v_lshrrev_b32_e32 v24, 2, v118
	s_addc_u32 s29, s43, 0
	s_lshl_b32 s6, s6, 6
	v_and_b32_e32 v2, 32, v2
	v_and_b32_e32 v24, 12, v24
	v_or3_b32 v2, v2, s6, v24
	v_or_b32_e32 v24, s17, v119
	v_add_u32_e32 v24, v24, v120
	v_ashrrev_i32_e32 v25, 31, v24
	v_lshlrev_b64 v[26:27], 10, v[24:25]
	v_mul_f32_e32 v25, 0xbfb8aa3b, v112
	v_exp_f32_e32 v25, v25
	v_lshl_add_u64 v[26:27], s[28:29], 0, v[26:27]
	v_lshlrev_b32_e32 v2, 1, v2
	v_lshl_add_u64 v[26:27], v[26:27], 0, v[2:3]
	v_add_f32_e32 v25, 1.0, v25
	v_rcp_f32_e32 v32, v25
	v_mul_f32_e32 v25, 0xbfb8aa3b, v113
	v_exp_f32_e32 v25, v25
	s_nop 0
	v_add_f32_e32 v25, 1.0, v25
	v_rcp_f32_e32 v33, v25
	v_mul_f32_e32 v25, 0xbfb8aa3b, v114
	v_exp_f32_e32 v25, v25
	v_pk_mul_f32 v[32:33], v[112:113], v[32:33]
	s_nop 0
	v_pk_mul_f32 v[32:33], v[108:109], v[32:33]
	v_add_f32_e32 v25, 1.0, v25
	v_rcp_f32_e32 v34, v25
	v_mul_f32_e32 v25, 0xbfb8aa3b, v115
	v_exp_f32_e32 v25, v25
	v_cvt_pk_bf16_f32 v32, v32, v33
	v_add_f32_e32 v25, 1.0, v25
	v_rcp_f32_e32 v35, v25
	v_mul_f32_e32 v25, 0xbfb8aa3b, v104
	v_exp_f32_e32 v25, v25
	v_pk_mul_f32 v[34:35], v[114:115], v[34:35]
	s_nop 0
	v_pk_mul_f32 v[34:35], v[110:111], v[34:35]
	v_add_f32_e32 v25, 1.0, v25
	v_cvt_pk_bf16_f32 v33, v34, v35
	global_store_dwordx2 v[26:27], v[32:33], off sc1
	v_rcp_f32_e32 v32, v25
	v_mul_f32_e32 v25, 0xbfb8aa3b, v105
	v_exp_f32_e32 v25, v25
	s_nop 0
	v_add_f32_e32 v25, 1.0, v25
	v_rcp_f32_e32 v33, v25
	v_mul_f32_e32 v25, 0xbfb8aa3b, v106
	v_exp_f32_e32 v25, v25
	v_pk_mul_f32 v[32:33], v[104:105], v[32:33]
	s_nop 0
	v_pk_mul_f32 v[32:33], v[100:101], v[32:33]
	v_add_f32_e32 v25, 1.0, v25
	v_rcp_f32_e32 v34, v25
	v_mul_f32_e32 v25, 0xbfb8aa3b, v107
	v_exp_f32_e32 v25, v25
	v_cvt_pk_bf16_f32 v32, v32, v33
	v_add_f32_e32 v25, 1.0, v25
; __device__ __forceinline__ float silu_f(float x) { return x * __builtin_amdgcn_rcpf(1.f + __expf(-x)); }
; __device__ __forceinline__ unsigned pk2bf(float lo, float hi) { const f32x2 v = {lo, hi}; return __builtin_bit_cast(unsigned, __builtin_convertvector(v, bf16x2_t)); }
; __device__ __forceinline__ void ph_moe1_mfma(const Ctx& c, int layer, int tile, const int* sm, unsigned char* lds) {
;     ...
; #pragma unroll
;     for (int m = 0; m < 4; ++m) {
;         const int rl = wr * 64 + m * 16 + fr;
; #pragma unroll
;         for (int n = 0; n < 2; ++n) {
;             const int col = nt * 64 + wc * 32 + n * 16 + fq * 4;
;             const f32x4 g = acc[m][n], u = acc[m][n + 2];
;             uint2 o; o.x = pk2bf(silu_f(g[0]) * u[0], silu_f(g[1]) * u[1]); o.y = pk2bf(silu_f(g[2]) * u[2], silu_f(g[3]) * u[3]);
;             __hip_atomic_store((unsigned long long*)(ACT + (size_t)(s0 + rl) * DE + col), ((unsigned long long)o.y << 32) | o.x, __ATOMIC_RELAXED, __HIP_MEMORY_SCOPE_AGENT);
;         }
;     }
;     asm volatile("s_waitcnt vmcnt(0)" ::: "memory");
;     __syncthreads();
;     if (c.tid == 0) (void)__hip_atomic_fetch_add(flag, 1u, __ATOMIC_RELAXED, __HIP_MEMORY_SCOPE_AGENT);
	v_rcp_f32_e32 v35, v25
	v_mul_f32_e32 v25, 0xbfb8aa3b, v96
	v_exp_f32_e32 v25, v25
	v_pk_mul_f32 v[34:35], v[106:107], v[34:35]
	s_nop 0
	v_pk_mul_f32 v[34:35], v[102:103], v[34:35]
	v_add_f32_e32 v25, 1.0, v25
	v_cvt_pk_bf16_f32 v33, v34, v35
	global_store_dwordx2 v[26:27], v[32:33], off offset:32 sc1
	v_rcp_f32_e32 v32, v25
	v_mul_f32_e32 v25, 0xbfb8aa3b, v97
	v_exp_f32_e32 v25, v25
	v_or_b32_e32 v26, 16, v24
	v_ashrrev_i32_e32 v27, 31, v26
	v_lshlrev_b64 v[26:27], 10, v[26:27]
	v_add_f32_e32 v25, 1.0, v25
	v_rcp_f32_e32 v33, v25
	v_mul_f32_e32 v25, 0xbfb8aa3b, v98
	v_exp_f32_e32 v25, v25
	v_lshl_add_u64 v[26:27], s[28:29], 0, v[26:27]
	v_pk_mul_f32 v[32:33], v[96:97], v[32:33]
	v_lshl_add_u64 v[26:27], v[26:27], 0, v[2:3]
	v_add_f32_e32 v25, 1.0, v25
	v_rcp_f32_e32 v34, v25
	v_mul_f32_e32 v25, 0xbfb8aa3b, v99
	v_exp_f32_e32 v25, v25
	v_pk_mul_f32 v[32:33], v[92:93], v[32:33]
	v_add_f32_e32 v25, 1.0, v25
	v_rcp_f32_e32 v35, v25
	v_mul_f32_e32 v25, 0xbfb8aa3b, v88
	v_exp_f32_e32 v25, v25
	v_cvt_pk_bf16_f32 v32, v32, v33
	v_pk_mul_f32 v[34:35], v[98:99], v[34:35]
	v_add_f32_e32 v25, 1.0, v25
	v_pk_mul_f32 v[34:35], v[94:95], v[34:35]
	s_nop 0
	v_cvt_pk_bf16_f32 v33, v34, v35
	global_store_dwordx2 v[26:27], v[32:33], off sc1
	v_rcp_f32_e32 v32, v25
	v_mul_f32_e32 v25, 0xbfb8aa3b, v89
	v_exp_f32_e32 v25, v25
	s_nop 0
	v_add_f32_e32 v25, 1.0, v25
	v_rcp_f32_e32 v33, v25
	v_mul_f32_e32 v25, 0xbfb8aa3b, v90
	v_exp_f32_e32 v25, v25
	v_pk_mul_f32 v[32:33], v[88:89], v[32:33]
	s_nop 0
	v_pk_mul_f32 v[32:33], v[84:85], v[32:33]
	v_add_f32_e32 v25, 1.0, v25
	v_rcp_f32_e32 v34, v25
	v_mul_f32_e32 v25, 0xbfb8aa3b, v91
	v_exp_f32_e32 v25, v25
	v_cvt_pk_bf16_f32 v32, v32, v33
	v_add_f32_e32 v25, 1.0, v25
	v_rcp_f32_e32 v35, v25
	v_mul_f32_e32 v25, 0xbfb8aa3b, v72
	v_exp_f32_e32 v25, v25
	v_pk_mul_f32 v[34:35], v[90:91], v[34:35]
	s_nop 0
	v_pk_mul_f32 v[34:35], v[86:87], v[34:35]
	v_add_f32_e32 v25, 1.0, v25
	v_cvt_pk_bf16_f32 v33, v34, v35
	global_store_dwordx2 v[26:27], v[32:33], off offset:32 sc1
	v_rcp_f32_e32 v32, v25
	v_mul_f32_e32 v25, 0xbfb8aa3b, v73
	v_exp_f32_e32 v25, v25
	v_or_b32_e32 v26, 32, v24
	v_ashrrev_i32_e32 v27, 31, v26
	v_lshlrev_b64 v[26:27], 10, v[26:27]
	v_add_f32_e32 v25, 1.0, v25
	v_rcp_f32_e32 v33, v25
	v_mul_f32_e32 v25, 0xbfb8aa3b, v74
	v_exp_f32_e32 v25, v25
	v_lshl_add_u64 v[26:27], s[28:29], 0, v[26:27]
	v_pk_mul_f32 v[32:33], v[72:73], v[32:33]
	v_lshl_add_u64 v[26:27], v[26:27], 0, v[2:3]
	v_add_f32_e32 v25, 1.0, v25
	v_rcp_f32_e32 v34, v25
	v_mul_f32_e32 v25, 0xbfb8aa3b, v75
	v_exp_f32_e32 v25, v25
	v_pk_mul_f32 v[32:33], v[60:61], v[32:33]
	v_add_f32_e32 v25, 1.0, v25
	v_rcp_f32_e32 v35, v25
	v_mul_f32_e32 v25, 0xbfb8aa3b, v28
	v_exp_f32_e32 v25, v25
	v_cvt_pk_bf16_f32 v32, v32, v33
	v_pk_mul_f32 v[34:35], v[74:75], v[34:35]
	v_add_f32_e32 v25, 1.0, v25
	v_pk_mul_f32 v[34:35], v[62:63], v[34:35]
	s_nop 0
	v_cvt_pk_bf16_f32 v33, v34, v35
	global_store_dwordx2 v[26:27], v[32:33], off sc1
	v_rcp_f32_e32 v32, v25
	v_mul_f32_e32 v25, 0xbfb8aa3b, v29
	v_exp_f32_e32 v25, v25
	s_nop 0
	v_add_f32_e32 v25, 1.0, v25
	v_rcp_f32_e32 v33, v25
	s_nop 0
	v_pk_mul_f32 v[28:29], v[28:29], v[32:33]
	s_nop 0
	v_pk_mul_f32 v[20:21], v[20:21], v[28:29]
	s_nop 0
	v_cvt_pk_bf16_f32 v20, v20, v21
	v_mul_f32_e32 v21, 0xbfb8aa3b, v30
	v_exp_f32_e32 v21, v21
	s_nop 0
	v_add_f32_e32 v21, 1.0, v21
	v_rcp_f32_e32 v28, v21
	v_mul_f32_e32 v21, 0xbfb8aa3b, v31
	v_exp_f32_e32 v21, v21
	s_nop 0
	v_add_f32_e32 v21, 1.0, v21
	v_rcp_f32_e32 v29, v21
	s_nop 0
	v_pk_mul_f32 v[28:29], v[30:31], v[28:29]
	s_nop 0
	v_pk_mul_f32 v[22:23], v[22:23], v[28:29]
	s_nop 0
	v_cvt_pk_bf16_f32 v21, v22, v23
	v_mul_f32_e32 v22, 0xbfb8aa3b, v12
	v_mul_f32_e32 v23, 0xbfb8aa3b, v13
	v_exp_f32_e32 v22, v22
	v_exp_f32_e32 v23, v23
	global_store_dwordx2 v[26:27], v[20:21], off offset:32 sc1
	v_or_b32_e32 v20, 48, v24
	v_add_f32_e32 v22, 1.0, v22
	v_add_f32_e32 v23, 1.0, v23
	v_rcp_f32_e32 v22, v22
	v_rcp_f32_e32 v23, v23
	v_ashrrev_i32_e32 v21, 31, v20
	v_lshlrev_b64 v[20:21], 10, v[20:21]
	v_lshl_add_u64 v[20:21], s[28:29], 0, v[20:21]
	v_pk_mul_f32 v[12:13], v[12:13], v[22:23]
	v_cmp_eq_u32_e64 s[28:29], 0, v118
	v_pk_mul_f32 v[12:13], v[16:17], v[12:13]
	s_nop 0
	v_cvt_pk_bf16_f32 v12, v12, v13
	v_mul_f32_e32 v13, 0xbfb8aa3b, v14
	v_exp_f32_e32 v13, v13
	s_nop 0
	v_add_f32_e32 v13, 1.0, v13
	v_rcp_f32_e32 v16, v13
	v_mul_f32_e32 v13, 0xbfb8aa3b, v15
	v_exp_f32_e32 v13, v13
	s_nop 0
	v_add_f32_e32 v13, 1.0, v13
	v_rcp_f32_e32 v17, v13
	s_nop 0
	v_pk_mul_f32 v[14:15], v[14:15], v[16:17]
	s_nop 0
	v_pk_mul_f32 v[14:15], v[18:19], v[14:15]
	s_nop 0
	v_cvt_pk_bf16_f32 v13, v14, v15
	v_lshl_add_u64 v[14:15], v[20:21], 0, v[2:3]
	v_mul_f32_e32 v2, 0xbfb8aa3b, v8
	v_exp_f32_e32 v2, v2
	global_store_dwordx2 v[14:15], v[12:13], off sc1
	v_add_f32_e32 v2, 1.0, v2
	v_rcp_f32_e32 v12, v2
	v_mul_f32_e32 v2, 0xbfb8aa3b, v9
	v_exp_f32_e32 v2, v2
	s_nop 0
	v_add_f32_e32 v2, 1.0, v2
	v_rcp_f32_e32 v13, v2
	v_mul_f32_e32 v2, 0xbfb8aa3b, v10
	v_exp_f32_e32 v2, v2
	v_pk_mul_f32 v[8:9], v[8:9], v[12:13]
	s_nop 0
	v_pk_mul_f32 v[4:5], v[4:5], v[8:9]
	v_add_f32_e32 v2, 1.0, v2
	v_rcp_f32_e32 v8, v2
	v_mul_f32_e32 v2, 0xbfb8aa3b, v11
	v_exp_f32_e32 v2, v2
	v_cvt_pk_bf16_f32 v4, v4, v5
	v_add_f32_e32 v2, 1.0, v2
	v_rcp_f32_e32 v9, v2
	s_nop 0
	v_pk_mul_f32 v[8:9], v[10:11], v[8:9]
	s_nop 0
	v_pk_mul_f32 v[6:7], v[6:7], v[8:9]
	s_nop 0
	v_cvt_pk_bf16_f32 v5, v6, v7
	global_store_dwordx2 v[14:15], v[4:5], off offset:32 sc1
	s_lshl_b32 s100, s16, 4
	s_add_i32 s100, s100, s57
	s_mov_b32 s101, 1
	s_branch .LBB0_136

; __device__ __forceinline__ void ph_moe1_mfma(const Ctx& c, int layer, int tile, const int* sm, unsigned char* lds) {
;     ...
;     asm volatile("s_waitcnt vmcnt(0)" ::: "memory");
;     __syncthreads();
;     if (c.tid == 0) (void)__hip_atomic_fetch_add(flag, 1u, __ATOMIC_RELAXED, __HIP_MEMORY_SCOPE_AGENT);
.LBB0_173:
	s_cmp_eq_u32 s101, 0
	s_cbranch_scc1 .Lm1_nopend3
	s_waitcnt vmcnt(0)
	s_barrier
	s_lshl_b32 s50, s100, 2
	s_add_u32 s50, s42, s50
	s_addc_u32 s51, s43, 0
	v_cmp_eq_u32_e32 vcc, 0, v118
	s_and_saveexec_b64 s[48:49], vcc
	v_mov_b32_e32 v2, 1
	global_atomic_add v221, v2, s[50:51]
	s_mov_b64 exec, s[48:49]
	s_mov_b32 s101, 0
